# P0 int8 activation row stores widened: 8 dword stores per row -> 2 dwordx4 stores via DPP quad transpose
# speedup vs baseline: 1.0026x; 1.0026x over previous
.LBB0_65:
	s_lshl_b32 s0, s96, 3
	s_add_i32 s0, s0, s86
	v_readlane_b32 s52, v254, 32
	s_cmpk_gt_i32 s0, 0x3fff
	v_readlane_b32 s53, v254, 33
	v_readlane_b32 s54, v254, 34
	v_readlane_b32 s55, v254, 35
	v_readlane_b32 s56, v254, 36
	v_readlane_b32 s57, v254, 37
	v_readlane_b32 s58, v254, 38
	v_readlane_b32 s59, v254, 39
	v_readlane_b32 s60, v254, 40
	v_readlane_b32 s61, v254, 41
	v_readlane_b32 s62, v254, 42
	v_readlane_b32 s63, v254, 43
	v_readlane_b32 s64, v254, 44
	v_readlane_b32 s65, v254, 45
	v_readlane_b32 s66, v254, 46
	v_readlane_b32 s67, v254, 47
	s_cbranch_scc1 .LBB0_70
	s_ashr_i32 s1, s0, 31
	s_lshl_b32 s4, s90, 3
	s_lshl_b64 s[8:9], s[0:1], 2
	s_add_u32 s3, s8, 0x181000
	s_addc_u32 s16, s9, 0
	s_ashr_i32 s5, s4, 31
	s_lshl_b64 s[10:11], s[0:1], 11
	s_lshl_b64 s[8:9], s[4:5], 2
	v_lshl_or_b32 v14, v1, 2, s10
	v_mov_b32_e32 v15, s11
	s_lshl_b64 s[10:11], s[4:5], 11
	s_lshl_b64 s[12:13], s[0:1], 13
	v_readlane_b32 s36, v254, 13
	v_readlane_b32 s37, v254, 14
	s_add_u32 s12, s36, s12
	v_lshlrev_b32_e32 v16, 4, v1
	v_mov_b32_e32 v17, 0
	s_addc_u32 s13, s37, s13
	v_lshl_add_u64 v[2:3], s[12:13], 0, v[16:17]
	s_mov_b64 s[12:13], 0x1000
	v_cmp_eq_u32_e64 s[6:7], 0, v1
	v_lshl_add_u64 v[18:19], v[2:3], 0, s[12:13]
	s_lshl_b64 s[12:13], s[4:5], 13
	s_mov_b32 s1, 0x42fe0000
	s_mov_b32 s5, 0x40c0c00
	s_mov_b32 s17, 0x5400000
	v_readlane_b32 s38, v254, 15
	v_readlane_b32 s39, v254, 16
	v_readlane_b32 s40, v254, 17
	v_readlane_b32 s41, v254, 18
	v_readlane_b32 s42, v254, 19
	v_readlane_b32 s43, v254, 20
	v_readlane_b32 s44, v254, 21
	v_readlane_b32 s45, v254, 22
	v_readlane_b32 s46, v254, 23
	v_readlane_b32 s47, v254, 24
	v_readlane_b32 s48, v254, 25
	v_readlane_b32 s49, v254, 26
	v_readlane_b32 s50, v254, 27
	v_readlane_b32 s51, v254, 28
	v_and_b32_e32 v60, 3, v1
	v_mul_u32_u24_e32 v60, 0xfc, v60
	v_add_u32_e32 v14, v14, v60
	s_branch .LBB0_68

.LBB0_68:
	global_load_dwordx4 v[20:23], v[18:19], off offset:-4096
	global_load_dwordx4 v[24:27], v[18:19], off offset:-3072
	global_load_dwordx4 v[28:31], v[18:19], off offset:-2048
	global_load_dwordx4 v[32:35], v[18:19], off offset:-1024
	global_load_dwordx4 v[36:39], v[18:19], off
	global_load_dwordx4 v[10:13], v[18:19], off offset:1024
	global_load_dwordx4 v[6:9], v[18:19], off offset:2048
	global_load_dwordx4 v[2:5], v[18:19], off offset:3072
	v_lshl_add_u64 v[40:41], s[92:93], 0, v[14:15]
	v_add_co_u32_e32 v40, vcc, s17, v40
	s_waitcnt vmcnt(7)
	v_max_f32_e64 v16, |v23|, |v23|
	v_max_f32_e64 v42, |v22|, |v22|
	s_waitcnt vmcnt(6)
	v_max_f32_e64 v43, |v27|, |v27|
	v_max_f32_e64 v44, |v26|, |v26|
	s_waitcnt vmcnt(5)
	v_max_f32_e64 v45, |v31|, |v31|
	v_max_f32_e64 v46, |v30|, |v30|
	s_waitcnt vmcnt(4)
	v_max_f32_e64 v47, |v35|, |v35|
	v_max_f32_e64 v48, |v34|, |v34|
	v_max_f32_e32 v16, v42, v16
	v_max_f32_e32 v42, v44, v43
	s_waitcnt vmcnt(3)
	v_max_f32_e64 v49, |v39|, |v39|
	v_max_f32_e64 v50, |v38|, |v38|
	s_waitcnt vmcnt(2)
	v_max_f32_e64 v51, |v13|, |v13|
	v_max_f32_e64 v52, |v12|, |v12|
	v_max_f32_e32 v43, v46, v45
	v_max_f32_e32 v44, v48, v47
	v_max3_f32 v16, |v20|, |v21|, v16
	v_max3_f32 v42, |v24|, |v25|, v42
	s_waitcnt vmcnt(1)
	v_max_f32_e64 v53, |v9|, |v9|
	v_max_f32_e64 v54, |v8|, |v8|
	s_waitcnt vmcnt(0)
	v_max_f32_e64 v55, |v5|, |v5|
	v_max_f32_e64 v56, |v4|, |v4|
	v_max_f32_e32 v45, v50, v49
	v_max_f32_e32 v46, v52, v51
	v_max3_f32 v43, |v28|, |v29|, v43
	v_max3_f32 v44, |v32|, |v33|, v44
	v_max3_f32 v16, v16, 0, v42
	v_max_f32_e32 v47, v54, v53
	v_max_f32_e32 v48, v56, v55
	v_max3_f32 v45, |v36|, |v37|, v45
	v_max3_f32 v46, |v10|, |v11|, v46
	v_max3_f32 v16, v16, v43, v44
	v_max3_f32 v47, |v6|, |v7|, v47
	v_max3_f32 v48, |v2|, |v3|, v48
	v_max3_f32 v16, v16, v45, v46
	v_max3_f32 v16, v16, v47, v48
	v_addc_co_u32_e32 v41, vcc, 0, v41, vcc
	s_nop 0
	v_mov_b32_dpp v42, v16 quad_perm:[1,0,3,2] row_mask:0xf bank_mask:0xf bound_ctrl:1
	v_max_f32_e32 v42, v42, v42
	v_max_f32_e32 v16, v16, v42
	s_nop 1
	v_mov_b32_dpp v42, v16 quad_perm:[2,3,0,1] row_mask:0xf bank_mask:0xf bound_ctrl:1
	v_max_f32_e32 v42, v42, v42
	v_max_f32_e32 v16, v16, v42
	s_nop 1
	v_mov_b32_dpp v42, v16 row_half_mirror row_mask:0xf bank_mask:0xf bound_ctrl:1
	v_max_f32_e32 v42, v42, v42
	v_max_f32_e32 v16, v16, v42
	s_nop 1
	v_mov_b32_dpp v42, v16 row_mirror row_mask:0xf bank_mask:0xf bound_ctrl:1
	v_max_f32_e32 v42, v42, v42
	v_max_f32_e32 v16, v16, v42
	v_mov_b32_e32 v42, v16
	s_nop 1
	v_permlane16_swap_b32_e32 v16, v42
	v_max_f32_e32 v42, v42, v42
	v_max_f32_e32 v16, v16, v16
	v_max_f32_e32 v16, v16, v42
	v_mov_b32_e32 v42, v16
	s_nop 1
	v_permlane32_swap_b32_e32 v16, v42
	v_max_f32_e32 v42, v42, v42
	v_max_f32_e32 v16, v16, v16
	v_max_f32_e32 v16, v16, v42
	v_div_scale_f32 v42, s[14:15], v16, v16, s1
	v_rcp_f32_e32 v43, v42
	v_div_scale_f32 v44, vcc, s1, v16, s1
	v_fma_f32 v45, -v42, v43, 1.0
	v_fmac_f32_e32 v43, v45, v43
	v_mul_f32_e32 v45, v44, v43
	v_fma_f32 v46, -v42, v45, v44
	v_fmac_f32_e32 v45, v46, v43
	v_fma_f32 v42, -v42, v45, v44
	v_div_fmas_f32 v42, v42, v43, v45
	v_div_fixup_f32 v42, v42, v16, s1
	v_cmp_lt_f32_e32 vcc, 0, v16
	s_nop 1
	v_cndmask_b32_e32 v42, 0, v42, vcc
	v_mul_f32_e32 v21, v21, v42
	v_mul_f32_e32 v20, v20, v42
	v_mul_f32_e32 v22, v22, v42
	v_mul_f32_e32 v23, v23, v42
	v_mul_f32_e32 v25, v25, v42
	v_rndne_f32_e32 v21, v21
	v_mul_f32_e32 v24, v24, v42
	v_mul_f32_e32 v26, v26, v42
	v_mul_f32_e32 v27, v27, v42
	v_rndne_f32_e32 v20, v20
	v_rndne_f32_e32 v22, v22
	v_rndne_f32_e32 v23, v23
	v_rndne_f32_e32 v25, v25
	v_cvt_i32_f32_e32 v21, v21
	v_rndne_f32_e32 v24, v24
	v_rndne_f32_e32 v26, v26
	v_rndne_f32_e32 v27, v27
	v_cvt_i32_f32_e32 v20, v20
	v_cvt_i32_f32_sdwa v22, v22 dst_sel:WORD_1 dst_unused:UNUSED_PAD src0_sel:DWORD
	v_cvt_i32_f32_e32 v23, v23
	v_cvt_i32_f32_e32 v25, v25
	v_cvt_i32_f32_e32 v24, v24
	v_cvt_i32_f32_sdwa v26, v26 dst_sel:WORD_1 dst_unused:UNUSED_PAD src0_sel:DWORD
	v_cvt_i32_f32_e32 v27, v27
	v_lshlrev_b32_e32 v21, 8, v21
	v_and_b32_e32 v22, 0xff0000, v22
	v_perm_b32 v20, v23, v20, s5
	v_lshlrev_b32_e32 v23, 8, v25
	v_and_b32_e32 v21, 0xff00, v21
	v_mul_f32_e32 v29, v29, v42
	v_and_b32_e32 v25, 0xff0000, v26
	v_perm_b32 v24, v27, v24, s5
	v_and_b32_e32 v23, 0xff00, v23
	v_or3_b32 v60, v20, v21, v22
	v_mul_f32_e32 v28, v28, v42
	v_mul_f32_e32 v30, v30, v42
	v_mul_f32_e32 v31, v31, v42
	v_or3_b32 v61, v24, v23, v25
	v_rndne_f32_e32 v20, v29
	v_rndne_f32_e32 v28, v28
	v_cvt_i32_f32_e32 v20, v20
	v_rndne_f32_e32 v21, v30
	v_rndne_f32_e32 v22, v31
	v_cvt_i32_f32_e32 v28, v28
	v_cvt_i32_f32_sdwa v21, v21 dst_sel:WORD_1 dst_unused:UNUSED_PAD src0_sel:DWORD
	v_cvt_i32_f32_e32 v22, v22
	v_lshlrev_b32_e32 v20, 8, v20
	v_and_b32_e32 v20, 0xff00, v20
	v_and_b32_e32 v21, 0xff0000, v21
	v_perm_b32 v22, v22, v28, s5
	v_or3_b32 v62, v22, v20, v21
	v_mul_f32_e32 v21, v33, v42
	v_mul_f32_e32 v20, v32, v42
	v_mul_f32_e32 v22, v34, v42
	v_mul_f32_e32 v23, v35, v42
	v_rndne_f32_e32 v21, v21
	v_rndne_f32_e32 v20, v20
	v_cvt_i32_f32_e32 v21, v21
	v_rndne_f32_e32 v22, v22
	v_rndne_f32_e32 v23, v23
	v_cvt_i32_f32_e32 v20, v20
	v_cvt_i32_f32_sdwa v22, v22 dst_sel:WORD_1 dst_unused:UNUSED_PAD src0_sel:DWORD
	v_cvt_i32_f32_e32 v23, v23
	v_lshlrev_b32_e32 v21, 8, v21
	v_and_b32_e32 v21, 0xff00, v21
	v_and_b32_e32 v22, 0xff0000, v22
	v_perm_b32 v20, v23, v20, s5
	v_or3_b32 v63, v20, v21, v22
	v_mul_f32_e32 v21, v37, v42
	v_mul_f32_e32 v11, v11, v42
	v_mul_f32_e32 v7, v7, v42
	v_mul_f32_e32 v3, v3, v42
	s_nop 1
	s_mov_b32 vcc_lo, 0x55555555
	s_mov_b32 vcc_hi, 0x55555555
	v_cndmask_b32_dpp v64, v61, v60, vcc quad_perm:[1,0,3,2] row_mask:0xf bank_mask:0xf
	v_cndmask_b32_dpp v65, v63, v62, vcc quad_perm:[1,0,3,2] row_mask:0xf bank_mask:0xf
	s_mov_b32 vcc_lo, 0xaaaaaaaa
	s_mov_b32 vcc_hi, 0xaaaaaaaa
	v_cndmask_b32_dpp v61, v60, v61, vcc quad_perm:[1,0,3,2] row_mask:0xf bank_mask:0xf
	v_cndmask_b32_dpp v63, v62, v63, vcc quad_perm:[1,0,3,2] row_mask:0xf bank_mask:0xf
	s_mov_b32 vcc_lo, 0x33333333
	s_mov_b32 vcc_hi, 0x33333333
	v_cndmask_b32_dpp v68, v65, v64, vcc quad_perm:[2,3,0,1] row_mask:0xf bank_mask:0xf
	v_cndmask_b32_dpp v69, v63, v61, vcc quad_perm:[2,3,0,1] row_mask:0xf bank_mask:0xf
	s_mov_b32 vcc_lo, 0xcccccccc
	s_mov_b32 vcc_hi, 0xcccccccc
	v_cndmask_b32_dpp v70, v64, v65, vcc quad_perm:[2,3,0,1] row_mask:0xf bank_mask:0xf
	v_cndmask_b32_dpp v71, v61, v63, vcc quad_perm:[2,3,0,1] row_mask:0xf bank_mask:0xf
	global_store_dwordx4 v[40:41], v[68:71], off
	v_mul_f32_e32 v20, v36, v42
	v_mul_f32_e32 v22, v38, v42
	v_mul_f32_e32 v23, v39, v42
	v_rndne_f32_e32 v21, v21
	v_mul_f32_e32 v10, v10, v42
	v_mul_f32_e32 v12, v12, v42
	v_mul_f32_e32 v13, v13, v42
	v_rndne_f32_e32 v11, v11
	v_mul_f32_e32 v6, v6, v42
	v_mul_f32_e32 v8, v8, v42
	v_mul_f32_e32 v9, v9, v42
	v_rndne_f32_e32 v7, v7
	v_mul_f32_e32 v2, v2, v42
	v_mul_f32_e32 v4, v4, v42
	v_mul_f32_e32 v5, v5, v42
	v_rndne_f32_e32 v3, v3
	v_rndne_f32_e32 v20, v20
	v_cvt_i32_f32_e32 v21, v21
	v_rndne_f32_e32 v22, v22
	v_rndne_f32_e32 v23, v23
	v_rndne_f32_e32 v10, v10
	v_cvt_i32_f32_e32 v11, v11
	v_rndne_f32_e32 v12, v12
	v_rndne_f32_e32 v13, v13
	v_rndne_f32_e32 v6, v6
	v_cvt_i32_f32_e32 v7, v7
	v_rndne_f32_e32 v8, v8
	v_rndne_f32_e32 v9, v9
	v_rndne_f32_e32 v2, v2
	v_cvt_i32_f32_e32 v3, v3
	v_rndne_f32_e32 v4, v4
	v_rndne_f32_e32 v5, v5
	v_cvt_i32_f32_e32 v20, v20
	v_cvt_i32_f32_sdwa v22, v22 dst_sel:WORD_1 dst_unused:UNUSED_PAD src0_sel:DWORD
	v_cvt_i32_f32_e32 v23, v23
	v_cvt_i32_f32_e32 v10, v10
	v_cvt_i32_f32_sdwa v12, v12 dst_sel:WORD_1 dst_unused:UNUSED_PAD src0_sel:DWORD
	v_cvt_i32_f32_e32 v13, v13
	v_cvt_i32_f32_e32 v6, v6
	v_cvt_i32_f32_sdwa v8, v8 dst_sel:WORD_1 dst_unused:UNUSED_PAD src0_sel:DWORD
	v_cvt_i32_f32_e32 v9, v9
	v_cvt_i32_f32_e32 v2, v2
	v_cvt_i32_f32_sdwa v4, v4 dst_sel:WORD_1 dst_unused:UNUSED_PAD src0_sel:DWORD
	v_cvt_i32_f32_e32 v5, v5
	v_lshlrev_b32_e32 v21, 8, v21
	v_lshlrev_b32_e32 v11, 8, v11
	v_lshlrev_b32_e32 v7, 8, v7
	v_lshlrev_b32_e32 v3, 8, v3
	v_and_b32_e32 v21, 0xff00, v21
	v_and_b32_e32 v22, 0xff0000, v22
	v_perm_b32 v20, v23, v20, s5
	v_and_b32_e32 v11, 0xff00, v11
	v_and_b32_e32 v12, 0xff0000, v12
	v_perm_b32 v10, v13, v10, s5
	v_and_b32_e32 v7, 0xff00, v7
	v_and_b32_e32 v8, 0xff0000, v8
	v_perm_b32 v6, v9, v6, s5
	v_and_b32_e32 v3, 0xff00, v3
	v_and_b32_e32 v4, 0xff0000, v4
	v_perm_b32 v2, v5, v2, s5
	v_or3_b32 v60, v20, v21, v22
	v_or3_b32 v61, v10, v11, v12
	v_or3_b32 v62, v6, v7, v8
	v_or3_b32 v63, v2, v3, v4
	s_nop 1
	s_mov_b32 vcc_lo, 0x55555555
	s_mov_b32 vcc_hi, 0x55555555
	v_cndmask_b32_dpp v64, v61, v60, vcc quad_perm:[1,0,3,2] row_mask:0xf bank_mask:0xf
	v_cndmask_b32_dpp v65, v63, v62, vcc quad_perm:[1,0,3,2] row_mask:0xf bank_mask:0xf
	s_mov_b32 vcc_lo, 0xaaaaaaaa
	s_mov_b32 vcc_hi, 0xaaaaaaaa
	v_cndmask_b32_dpp v61, v60, v61, vcc quad_perm:[1,0,3,2] row_mask:0xf bank_mask:0xf
	v_cndmask_b32_dpp v63, v62, v63, vcc quad_perm:[1,0,3,2] row_mask:0xf bank_mask:0xf
	s_mov_b32 vcc_lo, 0x33333333
	s_mov_b32 vcc_hi, 0x33333333
	v_cndmask_b32_dpp v68, v65, v64, vcc quad_perm:[2,3,0,1] row_mask:0xf bank_mask:0xf
	v_cndmask_b32_dpp v69, v63, v61, vcc quad_perm:[2,3,0,1] row_mask:0xf bank_mask:0xf
	s_mov_b32 vcc_lo, 0xcccccccc
	s_mov_b32 vcc_hi, 0xcccccccc
	v_cndmask_b32_dpp v70, v64, v65, vcc quad_perm:[2,3,0,1] row_mask:0xf bank_mask:0xf
	v_cndmask_b32_dpp v71, v61, v63, vcc quad_perm:[2,3,0,1] row_mask:0xf bank_mask:0xf
	global_store_dwordx4 v[40:41], v[68:71], off offset:1024
	s_and_saveexec_b64 s[14:15], s[6:7]
	s_cbranch_execz .LBB0_67
	s_add_u32 s18, s92, s3
	s_addc_u32 s19, s93, s16
	v_mul_f32_e32 v2, 0x3c010204, v16
	global_store_dword v17, v2, s[18:19]
	s_branch .LBB0_67
